# conversion row B requested behind the token tail's own loads; the tail's waits leave those 16 requests in flight
# baseline (speedup 1.0000x reference)
.LBB0_1127:
	s_or_b64 exec, exec, s[0:1]
	v_ashrrev_i32_e32 v34, 2, v151
	s_lshl_b64 s[0:1], s[96:97], 6
	v_ashrrev_i32_e32 v35, 31, v34
	s_add_u32 s0, s72, s0
	s_addc_u32 s1, s73, s1
	v_lshlrev_b64 v[36:37], 2, v[34:35]
	v_lshl_add_u64 v[38:39], s[0:1], 0, v[36:37]
	s_add_u32 s0, s96, 0x2000
	s_addc_u32 s1, s97, 0
	s_lshl_b64 s[2:3], s[0:1], 6
	s_add_u32 s2, s72, s2
	s_addc_u32 s3, s73, s3
	s_add_u32 s4, s96, 0x4000
	s_addc_u32 s5, s97, 0
	v_lshl_add_u64 v[40:41], s[2:3], 0, v[36:37]
	s_lshl_b64 s[2:3], s[4:5], 6
	s_add_u32 s2, s72, s2
	s_addc_u32 s3, s73, s3
	v_lshl_add_u64 v[36:37], s[2:3], 0, v[36:37]
	global_load_dword v43, v[38:39], off
	global_load_dword v69, v[40:41], off
	global_load_dword v70, v[36:37], off
	v_div_scale_f32 v46, s[2:3], v179, v179, 1.0
	v_rcp_f32_e32 v47, v46
	s_lshl_b64 s[2:3], s[96:97], 12
	s_add_u32 s6, s86, s2
	v_lshlrev_b32_e32 v44, 7, v34
	v_fma_f32 v35, -v46, v47, 1.0
	v_fmac_f32_e32 v47, v35, v47
	v_lshlrev_b32_e32 v35, 5, v151
	s_addc_u32 s7, s87, s3
	v_ashrrev_i32_e32 v45, 31, v44
	s_lshl_b64 s[0:1], s[0:1], 12
	v_and_b32_e32 v42, 0x60, v35
	v_lshlrev_b64 v[34:35], 1, v[44:45]
	s_add_u32 s0, s86, s0
	v_lshl_add_u64 v[36:37], s[6:7], 0, v[34:35]
	v_lshlrev_b32_e32 v146, 1, v42
	s_addc_u32 s1, s87, s1
	v_div_scale_f32 v48, vcc, 1.0, v179, 1.0
	s_waitcnt vmcnt(5)
	v_lshl_add_u64 v[62:63], v[36:37], 0, v[146:147]
	v_lshl_add_u64 v[36:37], s[0:1], 0, v[34:35]
	s_lshl_b64 s[0:1], s[4:5], 12
	v_mul_f32_e32 v49, v48, v47
	s_add_u32 s0, s86, s0
	s_waitcnt vmcnt(4)
	v_fma_f32 v50, -v46, v49, v48
	s_addc_u32 s1, s87, s1
	v_fmac_f32_e32 v49, v50, v47
	v_lshl_add_u64 v[34:35], s[0:1], 0, v[34:35]
	v_fma_f32 v46, -v46, v49, v48
	v_lshl_add_u64 v[64:65], v[36:37], 0, v[146:147]
	v_lshl_add_u64 v[66:67], v[34:35], 0, v[146:147]
	global_load_dwordx4 v[74:77], v[62:63], off
	global_load_dwordx4 v[34:37], v[62:63], off offset:48
	global_load_dwordx4 v[78:81], v[64:65], off
	global_load_dwordx4 v[38:41], v[64:65], off offset:48
	global_load_dwordx4 v[82:85], v[66:67], off
	v_div_fmas_f32 v46, v46, v47, v49
	v_div_fixup_f32 v68, v46, v179, 1.0
	global_load_dwordx4 v[86:89], v[62:63], off offset:32
	global_load_dwordx4 v[90:93], v[62:63], off offset:16
	global_load_dwordx4 v[94:97], v[64:65], off offset:32
	global_load_dwordx4 v[98:101], v[64:65], off offset:16
	global_load_dwordx4 v[102:105], v[66:67], off offset:32
	global_load_dwordx4 v[106:109], v[66:67], off offset:16
	s_waitcnt vmcnt(12)
	v_pk_mul_f32 v[58:59], v[4:5], v[68:69] op_sel_hi:[1,0]
	v_pk_mul_f32 v[54:55], v[8:9], v[68:69] op_sel_hi:[1,0]
	v_pk_mul_f32 v[60:61], v[2:3], v[68:69] op_sel_hi:[1,0]
	v_max_f32_e64 v2, |v58|, |v59|
	v_pk_mul_f32 v[56:57], v[6:7], v[68:69] op_sel_hi:[1,0]
	v_max_f32_e64 v3, |v54|, |v55|
	v_max3_f32 v2, |v60|, |v61|, v2
	v_max3_f32 v3, |v56|, |v57|, v3
	v_pk_mul_f32 v[50:51], v[12:13], v[68:69] op_sel_hi:[1,0]
	v_pk_mul_f32 v[46:47], v[16:17], v[68:69] op_sel_hi:[1,0]
	v_max3_f32 v2, v2, 0, v3
	v_pk_mul_f32 v[52:53], v[10:11], v[68:69] op_sel_hi:[1,0]
	v_max_f32_e64 v3, |v50|, |v51|
	v_pk_mul_f32 v[48:49], v[14:15], v[68:69] op_sel_hi:[1,0]
	v_max_f32_e64 v4, |v46|, |v47|
	v_max3_f32 v3, |v52|, |v53|, v3
	v_max3_f32 v4, |v48|, |v49|, v4
	v_pk_mul_f32 v[20:21], v[20:21], v[68:69] op_sel_hi:[1,0]
	v_pk_mul_f32 v[14:15], v[24:25], v[68:69] op_sel_hi:[1,0]
	v_max3_f32 v2, v2, v3, v4
	v_pk_mul_f32 v[18:19], v[18:19], v[68:69] op_sel_hi:[1,0]
	v_max_f32_e64 v3, |v20|, |v21|
	v_pk_mul_f32 v[16:17], v[22:23], v[68:69] op_sel_hi:[1,0]
	v_max_f32_e64 v4, |v14|, |v15|
	v_max3_f32 v3, |v18|, |v19|, v3
	v_max3_f32 v4, |v16|, |v17|, v4
	v_max3_f32 v2, v2, v3, v4
	s_waitcnt vmcnt(11)
	v_max3_f32 v4, v43, v69, v70
	v_sub_f32_e32 v5, v43, v4
	v_exp_f32_e32 v110, v5
	v_sub_f32_e32 v5, v69, v4
	v_exp_f32_e32 v5, v5
	v_sub_f32_e32 v4, v70, v4
	v_exp_f32_e32 v111, v4
	v_pk_mul_f32 v[10:11], v[32:33], v[68:69] op_sel_hi:[1,0]
	v_add_f32_e32 v4, v110, v5
	v_pk_mul_f32 v[6:7], v[28:29], v[68:69] op_sel_hi:[1,0]
	v_add_f32_e32 v4, v111, v4
	v_div_scale_f32 v22, s[0:1], v4, v4, 1.0
	v_rcp_f32_e32 v23, v22
	v_pk_mul_f32 v[12:13], v[30:31], v[68:69] op_sel_hi:[1,0]
	v_max_f32_e64 v3, |v10|, |v11|
	v_pk_mul_f32 v[8:9], v[26:27], v[68:69] op_sel_hi:[1,0]
	v_max_f32_e64 v24, |v6|, |v7|
	v_max3_f32 v3, |v12|, |v13|, v3
	v_max3_f32 v24, |v8|, |v9|, v24
	v_max3_f32 v43, v2, v3, v24
	v_fma_f32 v2, -v22, v23, 1.0
	v_fmac_f32_e32 v23, v2, v23
	v_div_scale_f32 v2, vcc, 1.0, v4, 1.0
	v_mul_f32_e32 v3, v2, v23
	v_fma_f32 v24, -v22, v3, v2
	v_fmac_f32_e32 v3, v24, v23
	v_fma_f32 v2, -v22, v3, v2
	v_div_fmas_f32 v2, v2, v23, v3
	v_div_fixup_f32 v112, v2, v4, 1.0
	v_mul_f32_e32 v113, v5, v112
	global_load_dwordx4 v[2:5], v[66:67], off offset:48
	s_add_i32 s30, s42, s40
	s_min_i32 s20, s30, 0x3fff
	s_lshl_b32 s20, s20, 14
	s_add_u32 s20, s48, s20
	s_addc_u32 s21, s49, 0
	v_lshlrev_b32_e32 v138, 4, v1
	global_load_dwordx4 v[180:183], v138, s[20:21] nt
	global_load_dwordx4 v[184:187], v138, s[20:21] offset:1024 nt
	global_load_dwordx4 v[188:191], v138, s[20:21] offset:2048 nt
	global_load_dwordx4 v[192:195], v138, s[20:21] offset:3072 nt
	s_add_u32 s20, s20, 0x1000
	s_addc_u32 s21, s21, 0
	global_load_dwordx4 v[196:199], v138, s[20:21] nt
	global_load_dwordx4 v[200:203], v138, s[20:21] offset:1024 nt
	global_load_dwordx4 v[204:207], v138, s[20:21] offset:2048 nt
	global_load_dwordx4 v[208:211], v138, s[20:21] offset:3072 nt
	s_add_u32 s20, s20, 0x1000
	s_addc_u32 s21, s21, 0
	global_load_dwordx4 v[212:215], v138, s[20:21] nt
	global_load_dwordx4 v[216:219], v138, s[20:21] offset:1024 nt
	global_load_dwordx4 v[220:223], v138, s[20:21] offset:2048 nt
	global_load_dwordx4 v[224:227], v138, s[20:21] offset:3072 nt
	s_add_u32 s20, s20, 0x1000
	s_addc_u32 s21, s21, 0
	global_load_dwordx4 v[228:231], v138, s[20:21] nt
	global_load_dwordx4 v[232:235], v138, s[20:21] offset:1024 nt
	global_load_dwordx4 v[236:239], v138, s[20:21] offset:2048 nt
	global_load_dwordx4 v[134:137], v138, s[20:21] offset:3072 nt
	s_waitcnt vmcnt(25)
	v_lshlrev_b32_e32 v22, 16, v78
	v_mul_f32_e32 v62, v113, v22
	v_and_b32_e32 v22, 0xffff0000, v78
	v_mul_f32_e32 v67, v113, v22
	v_lshlrev_b32_e32 v22, 16, v79
	v_mul_f32_e32 v71, v113, v22
	v_and_b32_e32 v22, 0xffff0000, v79
	s_waitcnt vmcnt(23)
	v_lshlrev_b32_e32 v115, 16, v82
	v_and_b32_e32 v78, 0xffff0000, v82
	v_lshlrev_b32_e32 v82, 16, v75
	v_and_b32_e32 v118, 0xffff0000, v75
	v_mul_f32_e32 v75, v113, v22
	v_lshlrev_b32_e32 v22, 16, v80
	v_mul_f32_e32 v32, v113, v22
	v_and_b32_e32 v22, 0xffff0000, v80
	v_mul_f32_e32 v66, v113, v22
	v_lshlrev_b32_e32 v22, 16, v81
	v_mul_f32_e32 v70, v113, v22
	v_and_b32_e32 v22, 0xffff0000, v81
	v_lshlrev_b32_e32 v114, 16, v74
	v_and_b32_e32 v116, 0xffff0000, v74
	v_mul_f32_e32 v74, v113, v22
	s_waitcnt vmcnt(19)
	v_lshlrev_b32_e32 v22, 16, v98
	v_mul_f32_e32 v31, v113, v22
	v_and_b32_e32 v22, 0xffff0000, v98
	v_mul_f32_e32 v65, v113, v22
	v_lshlrev_b32_e32 v22, 16, v99
	v_mul_f32_e32 v69, v113, v22
	v_and_b32_e32 v22, 0xffff0000, v99
	v_mul_f32_e32 v73, v113, v22
	v_lshlrev_b32_e32 v22, 16, v100
	v_mul_f32_e32 v29, v113, v22
	v_and_b32_e32 v22, 0xffff0000, v100
	v_mul_f32_e32 v63, v113, v22
	v_lshlrev_b32_e32 v22, 16, v101
	v_mul_f32_e32 v68, v113, v22
	v_and_b32_e32 v22, 0xffff0000, v101
	v_mul_f32_e32 v72, v113, v22
	v_lshlrev_b32_e32 v22, 16, v94
	v_mul_f32_e32 v24, v113, v22
	v_and_b32_e32 v22, 0xffff0000, v94
	v_mul_f32_e32 v27, v113, v22
	v_lshlrev_b32_e32 v22, 16, v95
	v_mul_f32_e32 v30, v113, v22
	v_and_b32_e32 v22, 0xffff0000, v95
	v_mul_f32_e32 v64, v113, v22
	v_lshlrev_b32_e32 v22, 16, v96
	v_mul_f32_e32 v23, v113, v22
	v_and_b32_e32 v22, 0xffff0000, v96
	v_mul_f32_e32 v26, v113, v22
	v_lshlrev_b32_e32 v22, 16, v97
	v_mul_f32_e32 v28, v113, v22
	v_and_b32_e32 v22, 0xffff0000, v97
	v_mul_f32_e32 v33, v113, v22
	v_lshlrev_b32_e32 v22, 16, v38
	v_and_b32_e32 v25, 0xffff0000, v38
	v_lshlrev_b32_e32 v130, 16, v39
	v_and_b32_e32 v131, 0xffff0000, v39
	v_pk_mul_f32 v[38:39], v[110:111], v[112:113] op_sel_hi:[1,0]
	v_lshlrev_b32_e32 v117, 16, v83
	v_and_b32_e32 v79, 0xffff0000, v83
	v_lshlrev_b32_e32 v83, 16, v76
	v_lshlrev_b32_e32 v119, 16, v84
	v_and_b32_e32 v76, 0xffff0000, v76
	v_and_b32_e32 v80, 0xffff0000, v84
	v_lshlrev_b32_e32 v84, 16, v77
	v_and_b32_e32 v77, 0xffff0000, v77
	v_fmac_f32_e32 v62, v38, v114
	v_fmac_f32_e32 v67, v38, v116
	v_fmac_f32_e32 v71, v38, v82
	v_fmac_f32_e32 v75, v38, v118
	v_lshlrev_b32_e32 v120, 16, v85
	v_and_b32_e32 v81, 0xffff0000, v85
	v_lshlrev_b32_e32 v85, 16, v90
	s_waitcnt vmcnt(17)
	v_lshlrev_b32_e32 v121, 16, v106
	v_and_b32_e32 v90, 0xffff0000, v90
	v_and_b32_e32 v98, 0xffff0000, v106
	v_lshlrev_b32_e32 v106, 16, v91
	v_and_b32_e32 v91, 0xffff0000, v91
	v_fmac_f32_e32 v62, v39, v115
	v_fmac_f32_e32 v67, v39, v78
	v_fmac_f32_e32 v71, v39, v117
	v_fmac_f32_e32 v75, v39, v79
	v_fmac_f32_e32 v32, v38, v83
	v_fmac_f32_e32 v66, v38, v76
	v_fmac_f32_e32 v70, v38, v84
	v_fmac_f32_e32 v74, v38, v77
	v_lshlrev_b32_e32 v122, 16, v107
	v_and_b32_e32 v99, 0xffff0000, v107
	v_lshlrev_b32_e32 v107, 16, v92
	v_lshlrev_b32_e32 v123, 16, v108
	v_and_b32_e32 v92, 0xffff0000, v92
	v_and_b32_e32 v100, 0xffff0000, v108
	v_lshlrev_b32_e32 v108, 16, v93
	v_and_b32_e32 v93, 0xffff0000, v93
	v_max_f32_e64 v78, |v62|, |v67|
	v_max_f32_e64 v79, |v71|, |v75|
	v_fmac_f32_e32 v32, v39, v119
	v_fmac_f32_e32 v66, v39, v80
	v_fmac_f32_e32 v70, v39, v120
	v_fmac_f32_e32 v74, v39, v81
	v_fmac_f32_e32 v31, v38, v85
	v_fmac_f32_e32 v65, v38, v90
	v_fmac_f32_e32 v69, v38, v106
	v_fmac_f32_e32 v73, v38, v91
	v_lshlrev_b32_e32 v124, 16, v109
	v_and_b32_e32 v101, 0xffff0000, v109
	v_lshlrev_b32_e32 v109, 16, v86
	v_lshlrev_b32_e32 v125, 16, v102
	v_and_b32_e32 v86, 0xffff0000, v86
	v_and_b32_e32 v94, 0xffff0000, v102
	v_lshlrev_b32_e32 v102, 16, v87
	v_and_b32_e32 v87, 0xffff0000, v87
	v_max3_f32 v43, v43, v78, v79
	v_max_f32_e64 v76, |v32|, |v66|
	v_max_f32_e64 v77, |v70|, |v74|
	v_fmac_f32_e32 v31, v39, v121
	v_fmac_f32_e32 v65, v39, v98
	v_fmac_f32_e32 v69, v39, v122
	v_fmac_f32_e32 v73, v39, v99
	v_fmac_f32_e32 v29, v38, v107
	v_fmac_f32_e32 v63, v38, v92
	v_fmac_f32_e32 v68, v38, v108
	v_fmac_f32_e32 v72, v38, v93
	v_lshlrev_b32_e32 v126, 16, v103
	v_and_b32_e32 v95, 0xffff0000, v103
	v_lshlrev_b32_e32 v103, 16, v88
	v_lshlrev_b32_e32 v127, 16, v104
	v_and_b32_e32 v88, 0xffff0000, v88
	v_and_b32_e32 v96, 0xffff0000, v104
	v_lshlrev_b32_e32 v104, 16, v89
	v_and_b32_e32 v89, 0xffff0000, v89
	v_max3_f32 v43, v43, v76, v77
	v_max_f32_e64 v76, |v31|, |v65|
	v_max_f32_e64 v77, |v69|, |v73|
	v_fmac_f32_e32 v29, v39, v123
	v_fmac_f32_e32 v63, v39, v100
	v_fmac_f32_e32 v68, v39, v124
	v_fmac_f32_e32 v72, v39, v101
	v_fmac_f32_e32 v24, v38, v109
	v_fmac_f32_e32 v27, v38, v86
	v_fmac_f32_e32 v30, v38, v102
	v_fmac_f32_e32 v64, v38, v87
	v_lshlrev_b32_e32 v128, 16, v105
	v_and_b32_e32 v97, 0xffff0000, v105
	v_max3_f32 v43, v43, v76, v77
	v_max_f32_e64 v76, |v29|, |v63|
	v_max_f32_e64 v77, |v68|, |v72|
	v_fmac_f32_e32 v24, v39, v125
	v_fmac_f32_e32 v27, v39, v94
	v_fmac_f32_e32 v30, v39, v126
	v_fmac_f32_e32 v64, v39, v95
	v_fmac_f32_e32 v23, v38, v103
	v_fmac_f32_e32 v26, v38, v88
	v_fmac_f32_e32 v28, v38, v104
	v_fmac_f32_e32 v33, v38, v89
	v_max3_f32 v43, v43, v76, v77
	v_max_f32_e64 v76, |v24|, |v27|
	v_max_f32_e64 v77, |v30|, |v64|
	v_fmac_f32_e32 v23, v39, v127
	v_fmac_f32_e32 v26, v39, v96
	v_fmac_f32_e32 v28, v39, v128
	v_fmac_f32_e32 v33, v39, v97
	v_max3_f32 v43, v43, v76, v77
	v_max_f32_e64 v76, |v23|, |v26|
	v_max_f32_e64 v77, |v28|, |v33|
	v_lshlrev_b32_e32 v105, 16, v34
	v_and_b32_e32 v34, 0xffff0000, v34
	v_mul_f32_e32 v25, v113, v25
	v_max3_f32 v43, v43, v76, v77
	s_waitcnt vmcnt(16)
	v_lshlrev_b32_e32 v77, 16, v3
	v_lshlrev_b32_e32 v76, 16, v35
	v_lshlrev_b32_e32 v129, 16, v2
	v_and_b32_e32 v2, 0xffff0000, v2
	v_fmac_f32_e32 v25, v38, v34
	v_pk_mul_f32 v[76:77], v[38:39], v[76:77]
	v_fmac_f32_e32 v25, v39, v2
	v_fma_f32 v2, v113, v130, v76
	v_add_f32_e32 v2, v2, v77
	v_and_b32_e32 v77, 0xffff0000, v3
	v_and_b32_e32 v76, 0xffff0000, v35
	v_mul_f32_e32 v22, v113, v22
	v_pk_mul_f32 v[34:35], v[38:39], v[76:77]
	v_fmac_f32_e32 v22, v38, v105
	v_fma_f32 v3, v113, v131, v34
	v_fmac_f32_e32 v22, v39, v129
	v_add_f32_e32 v34, v3, v35
	v_lshlrev_b32_e32 v77, 16, v4
	v_lshlrev_b32_e32 v76, 16, v36
	v_lshlrev_b32_e32 v132, 16, v40
	v_max_f32_e64 v78, |v22|, |v25|
	v_max_f32_e64 v3, |v2|, |v34|
	v_pk_mul_f32 v[76:77], v[38:39], v[76:77]
	v_max3_f32 v43, v43, v78, v3
	v_fma_f32 v3, v113, v132, v76
	v_add_f32_e32 v3, v3, v77
	v_and_b32_e32 v77, 0xffff0000, v4
	v_and_b32_e32 v76, 0xffff0000, v36
	v_and_b32_e32 v40, 0xffff0000, v40
	v_pk_mul_f32 v[76:77], v[38:39], v[76:77]
	v_lshlrev_b32_e32 v133, 16, v41
	v_fma_f32 v4, v113, v40, v76
	v_add_f32_e32 v4, v4, v77
	v_lshlrev_b32_e32 v77, 16, v5
	v_lshlrev_b32_e32 v76, 16, v37
	v_pk_mul_f32 v[76:77], v[38:39], v[76:77]
	v_and_b32_e32 v40, 0xffff0000, v37
	v_fma_f32 v35, v113, v133, v76
	v_and_b32_e32 v76, 0xffff0000, v41
	v_and_b32_e32 v41, 0xffff0000, v5
	v_pk_mul_f32 v[36:37], v[38:39], v[40:41]
	v_add_f32_e32 v35, v35, v77
	v_fma_f32 v5, v113, v76, v36
	v_add_f32_e32 v5, v5, v37
	v_max_f32_e64 v78, |v3|, |v4|
	v_max_f32_e64 v36, |v35|, |v5|
	v_max3_f32 v36, v43, v78, v36
	v_cmp_eq_u32_e32 vcc, 0, v151
	s_nop 0
	v_max_f32_dpp v36, v36, v36 quad_perm:[1,0,3,2] row_mask:0xf bank_mask:0xf
	s_nop 1
	v_max_f32_dpp v36, v36, v36 quad_perm:[2,3,0,1] row_mask:0xf bank_mask:0xf
	s_nop 1
	v_max_f32_dpp v36, v36, v36 row_half_mirror row_mask:0xf bank_mask:0xf
	s_nop 1
	v_max_f32_dpp v36, v36, v36 row_mirror row_mask:0xf bank_mask:0xf
	s_nop 1
	v_mov_b32_e32 v37, v36
	s_nop 1
	v_permlane16_swap_b32_e32 v36, v37
	v_max_f32_e32 v36, v36, v37
	v_mov_b32_e32 v37, v36
	s_nop 1
	v_permlane32_swap_b32_e32 v36, v37
	v_max_f32_e32 v36, v36, v37
	v_cmp_lt_f32_e64 s[0:1], 0, v36
	s_and_saveexec_b64 s[4:5], vcc
	s_cbranch_execz .LBB0_1129
	s_lshl_b64 s[6:7], s[96:97], 2
	v_readlane_b32 s8, v242, 39
	v_readlane_b32 s9, v242, 40
	s_add_u32 s6, s8, s6
	v_mul_f32_e32 v37, 0x3c010204, v36
	s_addc_u32 s7, s9, s7
	v_cndmask_b32_e64 v37, 1.0, v37, s[0:1]
	global_store_dword v147, v37, s[6:7]
